# EpiKvqNorm (kvq GEMM epilogue): the 15 per-store vmcnt(0) waits that only drained the previous store removed (serialised store ladder); stacked on peeled K-loops
# baseline (speedup 1.0000x reference)
.LBB0_1074:
	v_lshl_add_u32 v200, s24, 8, v155
	v_lshl_or_b32 v178, s22, 8, v191
	v_mov_b64_e32 v[150:151], s[96:97]
	v_ashrrev_i32_e32 v179, 31, v178
	v_mad_i64_i32 v[150:151], s[8:9], v200, s78, v[150:151]
	v_lshl_add_u64 v[186:187], v[178:179], 1, v[150:151]
	v_cvt_pk_bf16_f32 v126, v126, v127
	v_cvt_pk_bf16_f32 v127, v128, v129
	v_cvt_pk_bf16_f32 v128, v122, v123
	v_cvt_pk_bf16_f32 v129, v124, v125
	s_and_b64 vcc, exec, s[4:5]
	global_store_dwordx4 v[186:187], v[126:129], off
	s_cbranch_vccnz .LBB0_1076
	v_pk_mul_f32 v[120:121], v[120:121], v[176:177] op_sel_hi:[1,0]
	v_pk_mul_f32 v[118:119], v[118:119], v[176:177] op_sel_hi:[1,0]
	v_pk_mul_f32 v[116:117], v[116:117], v[176:177] op_sel_hi:[1,0]
	v_pk_mul_f32 v[114:115], v[114:115], v[176:177] op_sel_hi:[1,0]
	v_pk_mul_f32 v[120:121], v[136:137], v[120:121]
	v_pk_mul_f32 v[118:119], v[134:135], v[118:119]
	v_pk_mul_f32 v[116:117], v[132:133], v[116:117]
	v_pk_mul_f32 v[114:115], v[130:131], v[114:115]
.LBB0_1076:
	v_cvt_pk_bf16_f32 v118, v118, v119
	v_cvt_pk_bf16_f32 v119, v120, v121
	v_cvt_pk_bf16_f32 v120, v114, v115
	v_cvt_pk_bf16_f32 v121, v116, v117
	s_and_b64 vcc, exec, s[4:5]
	global_store_dwordx4 v[186:187], v[118:121], off offset:256
	s_cbranch_vccnz .LBB0_1078
	v_pk_mul_f32 v[112:113], v[112:113], v[174:175] op_sel_hi:[1,0]
	v_pk_mul_f32 v[110:111], v[110:111], v[174:175] op_sel_hi:[1,0]
	v_pk_mul_f32 v[108:109], v[108:109], v[174:175] op_sel_hi:[1,0]
	v_pk_mul_f32 v[106:107], v[106:107], v[174:175] op_sel_hi:[1,0]
	v_pk_mul_f32 v[112:113], v[136:137], v[112:113]
	v_pk_mul_f32 v[110:111], v[134:135], v[110:111]
	v_pk_mul_f32 v[108:109], v[108:109], v[132:133]
	v_pk_mul_f32 v[106:107], v[106:107], v[130:131]
.LBB0_1078:
	v_or_b32_e32 v116, 16, v200
	v_mov_b64_e32 v[114:115], s[96:97]
	v_mad_i64_i32 v[114:115], s[8:9], v116, s78, v[114:115]
	v_lshl_add_u64 v[114:115], v[178:179], 1, v[114:115]
	v_cvt_pk_bf16_f32 v110, v110, v111
	v_cvt_pk_bf16_f32 v111, v112, v113
	v_cvt_pk_bf16_f32 v112, v106, v107
	v_cvt_pk_bf16_f32 v113, v108, v109
	s_and_b64 vcc, exec, s[4:5]
	global_store_dwordx4 v[114:115], v[110:113], off
	s_cbranch_vccnz .LBB0_1080
	v_pk_mul_f32 v[104:105], v[104:105], v[172:173] op_sel_hi:[1,0]
	v_pk_mul_f32 v[102:103], v[102:103], v[172:173] op_sel_hi:[1,0]
	v_pk_mul_f32 v[100:101], v[100:101], v[172:173] op_sel_hi:[1,0]
	v_pk_mul_f32 v[98:99], v[98:99], v[172:173] op_sel_hi:[1,0]
	v_pk_mul_f32 v[104:105], v[104:105], v[136:137]
	v_pk_mul_f32 v[102:103], v[102:103], v[134:135]
	v_pk_mul_f32 v[100:101], v[100:101], v[132:133]
	v_pk_mul_f32 v[98:99], v[98:99], v[130:131]
.LBB0_1080:
	v_cvt_pk_bf16_f32 v102, v102, v103
	v_cvt_pk_bf16_f32 v103, v104, v105
	v_cvt_pk_bf16_f32 v104, v98, v99
	v_cvt_pk_bf16_f32 v105, v100, v101
	s_and_b64 vcc, exec, s[4:5]
	global_store_dwordx4 v[114:115], v[102:105], off offset:256
	s_cbranch_vccnz .LBB0_1082
	v_pk_mul_f32 v[96:97], v[96:97], v[170:171] op_sel_hi:[1,0]
	v_pk_mul_f32 v[94:95], v[94:95], v[170:171] op_sel_hi:[1,0]
	v_pk_mul_f32 v[92:93], v[92:93], v[170:171] op_sel_hi:[1,0]
	v_pk_mul_f32 v[90:91], v[90:91], v[170:171] op_sel_hi:[1,0]
	v_pk_mul_f32 v[96:97], v[96:97], v[136:137]
	v_pk_mul_f32 v[94:95], v[94:95], v[134:135]
	v_pk_mul_f32 v[92:93], v[92:93], v[132:133]
	v_pk_mul_f32 v[90:91], v[90:91], v[130:131]
.LBB0_1082:
	v_or_b32_e32 v100, 32, v200
	v_mov_b64_e32 v[98:99], s[96:97]
	v_mad_i64_i32 v[98:99], s[8:9], v100, s78, v[98:99]
	v_lshl_add_u64 v[98:99], v[178:179], 1, v[98:99]
	v_cvt_pk_bf16_f32 v94, v94, v95
	v_cvt_pk_bf16_f32 v95, v96, v97
	v_cvt_pk_bf16_f32 v96, v90, v91
	v_cvt_pk_bf16_f32 v97, v92, v93
	s_and_b64 vcc, exec, s[4:5]
	global_store_dwordx4 v[98:99], v[94:97], off
	s_cbranch_vccnz .LBB0_1084
	v_pk_mul_f32 v[88:89], v[88:89], v[168:169] op_sel_hi:[1,0]
	v_pk_mul_f32 v[86:87], v[86:87], v[168:169] op_sel_hi:[1,0]
	v_pk_mul_f32 v[84:85], v[84:85], v[168:169] op_sel_hi:[1,0]
	v_pk_mul_f32 v[82:83], v[82:83], v[168:169] op_sel_hi:[1,0]
	v_pk_mul_f32 v[88:89], v[88:89], v[136:137]
	v_pk_mul_f32 v[86:87], v[86:87], v[134:135]
	v_pk_mul_f32 v[84:85], v[84:85], v[132:133]
	v_pk_mul_f32 v[82:83], v[82:83], v[130:131]
.LBB0_1084:
	v_cvt_pk_bf16_f32 v86, v86, v87
	v_cvt_pk_bf16_f32 v87, v88, v89
	v_cvt_pk_bf16_f32 v88, v82, v83
	v_cvt_pk_bf16_f32 v89, v84, v85
	s_and_b64 vcc, exec, s[4:5]
	global_store_dwordx4 v[98:99], v[86:89], off offset:256
	s_cbranch_vccnz .LBB0_1086
	v_pk_mul_f32 v[80:81], v[80:81], v[166:167] op_sel_hi:[1,0]
	v_pk_mul_f32 v[78:79], v[78:79], v[166:167] op_sel_hi:[1,0]
	v_pk_mul_f32 v[76:77], v[76:77], v[166:167] op_sel_hi:[1,0]
	v_pk_mul_f32 v[74:75], v[74:75], v[166:167] op_sel_hi:[1,0]
	v_pk_mul_f32 v[80:81], v[80:81], v[136:137]
	v_pk_mul_f32 v[78:79], v[78:79], v[134:135]
	v_pk_mul_f32 v[76:77], v[76:77], v[132:133]
	v_pk_mul_f32 v[74:75], v[74:75], v[130:131]
.LBB0_1086:
	v_or_b32_e32 v84, 48, v200
	v_mov_b64_e32 v[82:83], s[96:97]
	v_mad_i64_i32 v[82:83], s[8:9], v84, s78, v[82:83]
	v_lshl_add_u64 v[82:83], v[178:179], 1, v[82:83]
	v_cvt_pk_bf16_f32 v78, v78, v79
	v_cvt_pk_bf16_f32 v79, v80, v81
	v_cvt_pk_bf16_f32 v80, v74, v75
	v_cvt_pk_bf16_f32 v81, v76, v77
	s_and_b64 vcc, exec, s[4:5]
	global_store_dwordx4 v[82:83], v[78:81], off
	s_cbranch_vccnz .LBB0_1088
	v_pk_mul_f32 v[72:73], v[72:73], v[164:165] op_sel_hi:[1,0]
	v_pk_mul_f32 v[70:71], v[70:71], v[164:165] op_sel_hi:[1,0]
	v_pk_mul_f32 v[68:69], v[68:69], v[164:165] op_sel_hi:[1,0]
	v_pk_mul_f32 v[66:67], v[66:67], v[164:165] op_sel_hi:[1,0]
	v_pk_mul_f32 v[72:73], v[72:73], v[136:137]
	v_pk_mul_f32 v[70:71], v[70:71], v[134:135]
	v_pk_mul_f32 v[68:69], v[68:69], v[132:133]
	v_pk_mul_f32 v[66:67], v[66:67], v[130:131]
.LBB0_1088:
	v_cvt_pk_bf16_f32 v70, v70, v71
	v_cvt_pk_bf16_f32 v71, v72, v73
	v_cvt_pk_bf16_f32 v72, v66, v67
	v_cvt_pk_bf16_f32 v73, v68, v69
	s_and_b64 vcc, exec, s[4:5]
	global_store_dwordx4 v[82:83], v[70:73], off offset:256
	s_cbranch_vccnz .LBB0_1090
	v_pk_mul_f32 v[64:65], v[64:65], v[162:163] op_sel_hi:[1,0]
	v_pk_mul_f32 v[62:63], v[62:63], v[162:163] op_sel_hi:[1,0]
	v_pk_mul_f32 v[60:61], v[60:61], v[162:163] op_sel_hi:[1,0]
	v_pk_mul_f32 v[58:59], v[58:59], v[162:163] op_sel_hi:[1,0]
	v_pk_mul_f32 v[64:65], v[64:65], v[136:137]
	v_pk_mul_f32 v[62:63], v[62:63], v[134:135]
	v_pk_mul_f32 v[60:61], v[60:61], v[132:133]
	v_pk_mul_f32 v[58:59], v[58:59], v[130:131]
.LBB0_1090:
	v_add_u32_e32 v68, 0x80, v200
	v_mov_b64_e32 v[66:67], s[96:97]
	v_mad_i64_i32 v[66:67], s[8:9], v68, s78, v[66:67]
	v_lshl_add_u64 v[66:67], v[178:179], 1, v[66:67]
	v_cvt_pk_bf16_f32 v62, v62, v63
	v_cvt_pk_bf16_f32 v63, v64, v65
	v_cvt_pk_bf16_f32 v64, v58, v59
	v_cvt_pk_bf16_f32 v65, v60, v61
	s_and_b64 vcc, exec, s[4:5]
	global_store_dwordx4 v[66:67], v[62:65], off
	s_cbranch_vccnz .LBB0_1092
	v_pk_mul_f32 v[56:57], v[56:57], v[160:161] op_sel_hi:[1,0]
	v_pk_mul_f32 v[54:55], v[54:55], v[160:161] op_sel_hi:[1,0]
	v_pk_mul_f32 v[52:53], v[52:53], v[160:161] op_sel_hi:[1,0]
	v_pk_mul_f32 v[50:51], v[50:51], v[160:161] op_sel_hi:[1,0]
	v_pk_mul_f32 v[56:57], v[56:57], v[136:137]
	v_pk_mul_f32 v[54:55], v[54:55], v[134:135]
	v_pk_mul_f32 v[52:53], v[52:53], v[132:133]
	v_pk_mul_f32 v[50:51], v[50:51], v[130:131]
.LBB0_1092:
	v_cvt_pk_bf16_f32 v54, v54, v55
	v_cvt_pk_bf16_f32 v55, v56, v57
	v_cvt_pk_bf16_f32 v56, v50, v51
	v_cvt_pk_bf16_f32 v57, v52, v53
	s_and_b64 vcc, exec, s[4:5]
	global_store_dwordx4 v[66:67], v[54:57], off offset:256
	s_cbranch_vccnz .LBB0_1094
	v_pk_mul_f32 v[48:49], v[48:49], v[158:159] op_sel_hi:[1,0]
	v_pk_mul_f32 v[46:47], v[46:47], v[158:159] op_sel_hi:[1,0]
	v_pk_mul_f32 v[44:45], v[44:45], v[158:159] op_sel_hi:[1,0]
	v_pk_mul_f32 v[42:43], v[42:43], v[158:159] op_sel_hi:[1,0]
	v_pk_mul_f32 v[48:49], v[48:49], v[136:137]
	v_pk_mul_f32 v[46:47], v[46:47], v[134:135]
	v_pk_mul_f32 v[44:45], v[44:45], v[132:133]
	v_pk_mul_f32 v[42:43], v[42:43], v[130:131]
.LBB0_1094:
	v_add_u32_e32 v52, 0x90, v200
	v_mov_b64_e32 v[50:51], s[96:97]
	v_mad_i64_i32 v[50:51], s[8:9], v52, s78, v[50:51]
	v_lshl_add_u64 v[50:51], v[178:179], 1, v[50:51]
	v_cvt_pk_bf16_f32 v46, v46, v47
	v_cvt_pk_bf16_f32 v47, v48, v49
	v_cvt_pk_bf16_f32 v48, v42, v43
	v_cvt_pk_bf16_f32 v49, v44, v45
	s_and_b64 vcc, exec, s[4:5]
	global_store_dwordx4 v[50:51], v[46:49], off
	s_cbranch_vccnz .LBB0_1096
	v_pk_mul_f32 v[40:41], v[40:41], v[156:157] op_sel_hi:[1,0]
	v_pk_mul_f32 v[38:39], v[38:39], v[156:157] op_sel_hi:[1,0]
	v_pk_mul_f32 v[36:37], v[36:37], v[156:157] op_sel_hi:[1,0]
	v_pk_mul_f32 v[34:35], v[34:35], v[156:157] op_sel_hi:[1,0]
	v_pk_mul_f32 v[40:41], v[40:41], v[136:137]
	v_pk_mul_f32 v[38:39], v[38:39], v[134:135]
	v_pk_mul_f32 v[36:37], v[36:37], v[132:133]
	v_pk_mul_f32 v[34:35], v[34:35], v[130:131]
.LBB0_1096:
	v_cvt_pk_bf16_f32 v38, v38, v39
	v_cvt_pk_bf16_f32 v39, v40, v41
	v_cvt_pk_bf16_f32 v40, v34, v35
	v_cvt_pk_bf16_f32 v41, v36, v37
	s_and_b64 vcc, exec, s[4:5]
	global_store_dwordx4 v[50:51], v[38:41], off offset:256
	s_cbranch_vccnz .LBB0_1098
	v_pk_mul_f32 v[32:33], v[32:33], v[154:155] op_sel_hi:[1,0]
	v_pk_mul_f32 v[30:31], v[30:31], v[154:155] op_sel_hi:[1,0]
	v_pk_mul_f32 v[28:29], v[28:29], v[154:155] op_sel_hi:[1,0]
	v_pk_mul_f32 v[26:27], v[26:27], v[154:155] op_sel_hi:[1,0]
	v_pk_mul_f32 v[32:33], v[32:33], v[136:137]
	v_pk_mul_f32 v[30:31], v[30:31], v[134:135]
	v_pk_mul_f32 v[28:29], v[28:29], v[132:133]
	v_pk_mul_f32 v[26:27], v[26:27], v[130:131]
.LBB0_1098:
	v_add_u32_e32 v36, 0xa0, v200
	v_mov_b64_e32 v[34:35], s[96:97]
	v_mad_i64_i32 v[34:35], s[8:9], v36, s78, v[34:35]
	v_lshl_add_u64 v[34:35], v[178:179], 1, v[34:35]
	v_cvt_pk_bf16_f32 v30, v30, v31
	v_cvt_pk_bf16_f32 v31, v32, v33
	v_cvt_pk_bf16_f32 v32, v26, v27
	v_cvt_pk_bf16_f32 v33, v28, v29
	s_and_b64 vcc, exec, s[4:5]
	global_store_dwordx4 v[34:35], v[30:33], off
	s_cbranch_vccnz .LBB0_1100
	v_pk_mul_f32 v[24:25], v[24:25], v[184:185] op_sel_hi:[1,0]
	v_pk_mul_f32 v[22:23], v[22:23], v[184:185] op_sel_hi:[1,0]
	v_pk_mul_f32 v[20:21], v[20:21], v[184:185] op_sel_hi:[1,0]
	v_pk_mul_f32 v[18:19], v[18:19], v[184:185] op_sel_hi:[1,0]
	v_pk_mul_f32 v[24:25], v[24:25], v[136:137]
	v_pk_mul_f32 v[22:23], v[22:23], v[134:135]
	v_pk_mul_f32 v[20:21], v[20:21], v[132:133]
	v_pk_mul_f32 v[18:19], v[18:19], v[130:131]
.LBB0_1100:
	v_cvt_pk_bf16_f32 v22, v22, v23
	v_cvt_pk_bf16_f32 v23, v24, v25
	v_cvt_pk_bf16_f32 v24, v18, v19
	v_cvt_pk_bf16_f32 v25, v20, v21
	s_and_b64 vcc, exec, s[4:5]
	global_store_dwordx4 v[34:35], v[22:25], off offset:256
	s_cbranch_vccnz .LBB0_1102
	v_pk_mul_f32 v[16:17], v[16:17], v[182:183] op_sel_hi:[1,0]
	v_pk_mul_f32 v[14:15], v[14:15], v[182:183] op_sel_hi:[1,0]
	v_pk_mul_f32 v[12:13], v[12:13], v[182:183] op_sel_hi:[1,0]
	v_pk_mul_f32 v[10:11], v[10:11], v[182:183] op_sel_hi:[1,0]
	v_pk_mul_f32 v[16:17], v[16:17], v[136:137]
	v_pk_mul_f32 v[14:15], v[14:15], v[134:135]
	v_pk_mul_f32 v[12:13], v[12:13], v[132:133]
	v_pk_mul_f32 v[10:11], v[10:11], v[130:131]
.LBB0_1102:
	v_add_u32_e32 v20, 0xb0, v200
	v_mov_b64_e32 v[18:19], s[96:97]
	v_mad_i64_i32 v[18:19], s[8:9], v20, s78, v[18:19]
	v_lshl_add_u64 v[18:19], v[178:179], 1, v[18:19]
	v_cvt_pk_bf16_f32 v14, v14, v15
	v_cvt_pk_bf16_f32 v15, v16, v17
	v_cvt_pk_bf16_f32 v16, v10, v11
	v_cvt_pk_bf16_f32 v17, v12, v13
	s_and_b64 vcc, exec, s[4:5]
	global_store_dwordx4 v[18:19], v[14:17], off
	s_cbranch_vccnz .LBB0_1033
	v_pk_mul_f32 v[8:9], v[8:9], v[180:181] op_sel_hi:[1,0]
	v_pk_mul_f32 v[6:7], v[6:7], v[180:181] op_sel_hi:[1,0]
	v_pk_mul_f32 v[4:5], v[4:5], v[180:181] op_sel_hi:[1,0]
	v_pk_mul_f32 v[2:3], v[2:3], v[180:181] op_sel_hi:[1,0]
	v_pk_mul_f32 v[8:9], v[8:9], v[136:137]
	v_pk_mul_f32 v[6:7], v[6:7], v[134:135]
	v_pk_mul_f32 v[4:5], v[4:5], v[132:133]
	v_pk_mul_f32 v[2:3], v[2:3], v[130:131]
	s_branch .LBB0_1033
